# attention unit loop: removed the branch skeleton and padding left around the deleted per-wave DMA blocks (branches that only skipped s_nop, their flag setup)
# speedup vs baseline: 1.0052x; 1.0052x over previous
.LBB0_429:
	v_writelane_b32 v254, s78, 15
	s_add_u32 s1, s6, 0x1400000
	s_mov_b32 s2, s90
	v_writelane_b32 v254, s79, 16
	v_writelane_b32 v254, s1, 17
	s_addc_u32 s1, s7, 0
	v_writelane_b32 v254, s1, 18
	v_lshlrev_b32_e32 v10, 1, v4
	v_writelane_b32 v254, s2, 19
	v_and_b32_e32 v10, 32, v10
	v_lshlrev_b32_e32 v11, 3, v4
	v_writelane_b32 v254, s3, 20
	s_add_i32 s1, s3, 32
	v_mov_b32_e32 v179, 0
	v_and_or_b32 v13, v11, 24, v10
	v_lshlrev_b32_e32 v10, 4, v4
	v_writelane_b32 v254, s1, 21
	s_or_b32 s1, s21, 0xffffff80
	v_and_b32_e32 v10, 0x70, v10
	v_mov_b32_e32 v11, v179
	v_writelane_b32 v254, s1, 22
	v_or_b32_e32 v192, s1, v5
	s_add_i32 s1, s3, 0xffffffa0
	v_lshl_add_u64 v[10:11], s[6:7], 0, v[10:11]
	s_mov_b64 s[4:5], 0x12000000
	v_writelane_b32 v254, s1, 23
	v_lshl_add_u64 v[184:185], v[10:11], 0, s[4:5]
	s_or_b32 s4, s3, 8
	v_writelane_b32 v254, s4, 24
	s_or_b32 s4, s3, 16
	v_writelane_b32 v254, s4, 25
	s_or_b32 s4, s3, 24
	v_writelane_b32 v254, s4, 26
	s_add_i32 s4, s3, 40
	v_writelane_b32 v254, s4, 27
	s_add_i32 s4, s3, 48
	v_writelane_b32 v254, s4, 28
	s_add_i32 s4, s3, 56
	v_writelane_b32 v254, s4, 29
	s_or_b32 s4, s21, 0xffffff88
	v_writelane_b32 v254, s4, 30
	s_or_b32 s4, s21, 0xffffff90
	v_writelane_b32 v254, s4, 31
	s_or_b32 s4, s21, 0xffffff98
	v_writelane_b32 v254, s4, 32
	s_add_i32 s4, s3, 0xffffffa8
	v_writelane_b32 v254, s4, 33
	s_add_i32 s4, s3, 0xffffffb0
	v_lshlrev_b32_e32 v12, 2, v6
	v_writelane_b32 v254, s4, 34
	s_add_i32 s4, s3, 0xffffffb8
	v_writelane_b32 v254, s4, 35
	v_cmp_gt_u32_e64 s[4:5], v12, v7
	v_or_b32_e32 v15, 1, v12
	v_cmp_lt_u32_e64 s[8:9], v12, v7
	v_writelane_b32 v254, s4, 36
	v_and_b32_e32 v3, 7, v4
	v_lshlrev_b32_e32 v193, 4, v3
	v_writelane_b32 v254, s5, 37
	v_cmp_lt_u32_e64 s[4:5], v15, v7
	v_or_b32_e32 v15, 2, v12
	v_lshlrev_b32_e32 v2, 3, v6
	v_writelane_b32 v254, s4, 38
	v_cmp_gt_u32_e64 s[6:7], 32, v8
	v_bitop3_b32 v8, v6, v4, 7 bitop3:0x78
	v_writelane_b32 v254, s5, 39
	v_cmp_lt_u32_e64 s[4:5], v15, v7
	v_bitop3_b32 v10, v6, v3, 2 bitop3:0x36
	v_bitop3_b32 v11, v6, v3, 4 bitop3:0x36
	v_writelane_b32 v254, s4, 40
	v_bitop3_b32 v3, v6, v3, 6 bitop3:0x36
	s_add_i32 s83, s75, 0x1000
	v_writelane_b32 v254, s5, 41
	v_cmp_gt_u32_e64 s[4:5], v15, v7
	v_or_b32_e32 v15, 3, v12
	v_or_b32_e32 v1, s3, v7
	v_writelane_b32 v254, s4, 42
	v_bitop3_b32 v9, v5, v4, 7 bitop3:0x78
	v_lshl_add_u32 v14, v7, 7, s75
	v_writelane_b32 v254, s5, 43
	v_cmp_lt_u32_e64 s[4:5], v15, v7
	v_or_b32_e32 v19, 8, v5
	s_lshl_b32 s22, s90, 2
	v_writelane_b32 v254, s4, 44
	v_lshl_add_u32 v18, v5, 7, s75
	v_or_b32_e32 v203, s3, v5
	v_writelane_b32 v254, s5, 45
	v_cmp_gt_u32_e64 s[4:5], v15, v7
	v_or_b32_e32 v15, 8, v12
	v_lshl_add_u32 v20, v19, 7, s75
	v_writelane_b32 v254, s4, 46
	v_or_b32_e32 v204, s3, v19
	v_or_b32_e32 v19, 16, v5
	v_writelane_b32 v254, s5, 47
	v_cmp_lt_u32_e64 s[4:5], v15, v7
	v_add_u32_e32 v194, v14, v2
	v_lshlrev_b32_e32 v8, 4, v8
	v_writelane_b32 v254, s4, 48
	v_lshlrev_b32_e32 v10, 4, v10
	v_lshlrev_b32_e32 v11, 4, v11
	v_writelane_b32 v254, s5, 49
	v_cmp_gt_u32_e64 s[4:5], v15, v7
	v_or_b32_e32 v15, 9, v12
	v_lshlrev_b32_e32 v3, 4, v3
	v_writelane_b32 v254, s4, 50
	v_xor_b32_e32 v16, 0x60, v193
	v_xor_b32_e32 v17, 0x70, v193
	v_writelane_b32 v254, s5, 51
	v_cmp_lt_u32_e64 s[4:5], v15, v7
	v_lshl_add_u32 v21, v19, 7, s75
	v_or_b32_e32 v205, s3, v19
	v_writelane_b32 v254, s4, 52
	v_lshlrev_b32_e32 v186, 1, v2
	v_mbcnt_lo_u32_b32 v2, -1, 0
	v_writelane_b32 v254, s5, 53
	v_cmp_gt_u32_e64 s[4:5], v15, v7
	v_or_b32_e32 v15, 10, v12
	s_xor_b32 s1, s3, 0x7f
	v_writelane_b32 v254, s4, 54
	s_add_i32 s2, s3, 64
	s_add_i32 s10, s3, 0x48
	v_writelane_b32 v254, s5, 55
	v_cmp_lt_u32_e64 s[4:5], v15, v7
	s_add_i32 s11, s3, 0x50
	s_add_i32 s12, s3, 0x58
	v_writelane_b32 v254, s4, 56
	s_add_i32 s13, s3, 0x60
	s_add_i32 s14, s3, 0x68
	v_writelane_b32 v254, s5, 57
	v_cmp_gt_u32_e64 s[4:5], v15, v7
	v_or_b32_e32 v15, 11, v12
	s_add_i32 s15, s3, 0x70
	v_writelane_b32 v254, s4, 58
	s_add_i32 s16, s3, 0x78
	s_or_b32 s17, s3, 0x80
	v_writelane_b32 v254, s5, 59
	v_cmp_lt_u32_e64 s[4:5], v15, v7
	s_or_b32 s18, s3, 0x88
	s_or_b32 s19, s3, 0x90
	v_writelane_b32 v254, s4, 60
	s_or_b32 s20, s3, 0x98
	v_or_b32_e32 v208, 0x1000, v193
	v_writelane_b32 v254, s5, 61
	v_cmp_gt_u32_e64 s[4:5], v15, v7
	v_or_b32_e32 v15, 16, v12
	s_mov_b32 s91, 0
	v_writelane_b32 v254, s4, 62
	s_movk_i32 s21, 0x1880
	s_mov_b64 s[92:93], 0x800
	v_writelane_b32 v254, s5, 63
	v_cmp_lt_u32_e64 s[4:5], v15, v7
	s_add_i32 s23, s75, 0x2400
	s_add_i32 s24, s75, 0x2800
	v_writelane_b32 v255, s4, 0
	s_add_i32 s25, s75, 0x2c00
	s_mov_b64 s[94:95], 0x1000
	v_writelane_b32 v255, s5, 1
	v_cmp_gt_u32_e64 s[4:5], v15, v7
	v_or_b32_e32 v15, 17, v12
	s_add_i32 s26, s75, 0x400
	v_writelane_b32 v255, s4, 2
	s_add_i32 s27, s75, 0xc00
	s_add_i32 s28, s75, 0x1400
	v_writelane_b32 v255, s5, 3
	v_cmp_lt_u32_e64 s[4:5], v15, v7
	s_add_i32 s29, s75, 0x1800
	s_add_i32 s30, s75, 0x1c00
	v_writelane_b32 v255, s4, 4
	s_add_i32 s31, s75, 0x3000
	s_add_i32 s34, s75, 0x3400
	v_writelane_b32 v255, s5, 5
	v_cmp_gt_u32_e64 s[4:5], v15, v7
	v_or_b32_e32 v15, 18, v12
	s_add_i32 s35, s75, 0x3800
	v_writelane_b32 v255, s4, 6
	s_add_i32 s36, s75, 0x3c00
	v_mbcnt_hi_u32_b32 v209, -1, v2
	v_writelane_b32 v255, s5, 7
	v_cmp_lt_u32_e64 s[4:5], v15, v7
	v_add_u32_e32 v215, v194, v16
	v_add_u32_e32 v216, v194, v17
	v_writelane_b32 v255, s4, 8
	v_add_u32_e32 v221, v14, v8
	v_add_u32_e32 v222, v14, v10
	v_writelane_b32 v255, s5, 9
	v_cmp_gt_u32_e64 s[4:5], v15, v7
	v_or_b32_e32 v15, 19, v12
	v_cmp_gt_u32_e64 s[54:55], v15, v7
	v_writelane_b32 v255, s4, 10
	v_add_u32_e32 v223, v14, v11
	v_add_u32_e32 v224, v14, v3
	v_writelane_b32 v255, s5, 11
	v_cmp_lt_u32_e64 s[4:5], v15, v7
	v_or_b32_e32 v15, 24, v12
	v_cmp_lt_u32_e64 s[56:57], v15, v7
	v_cmp_gt_u32_e64 s[58:59], v15, v7
	v_or_b32_e32 v15, 25, v12
	v_cmp_lt_u32_e64 s[60:61], v15, v7
	v_cmp_gt_u32_e64 s[62:63], v15, v7
	v_or_b32_e32 v15, 26, v12
	v_or_b32_e32 v12, 27, v12
	v_cmp_lt_u32_e64 s[68:69], v12, v7
	v_cmp_gt_u32_e64 s[70:71], v12, v7
	v_lshlrev_b32_e32 v12, 5, v4
	v_and_b32_e32 v12, 0x180, v12
	v_lshl_or_b32 v6, v6, 9, v12
	v_cmp_lt_u32_e64 s[64:65], v15, v7
	v_cmp_gt_u32_e64 s[66:67], v15, v7
	v_add_u32_e32 v7, s75, v13
	v_or_b32_e32 v12, 0x800, v6
	v_xor_b32_e32 v4, v5, v4
	v_writelane_b32 v255, s4, 12
	v_add_u32_e32 v195, v7, v6
	v_add_u32_e32 v197, v12, v7
	v_add_u32_e32 v7, s83, v13
	v_lshlrev_b32_e32 v4, 4, v4
	v_or_b32_e32 v5, 24, v5
	v_writelane_b32 v255, s5, 13
	v_add_u32_e32 v199, v7, v6
	v_add_u32_e32 v201, v7, v12
	v_xor_b32_e32 v6, 16, v193
	v_xor_b32_e32 v7, 32, v193
	v_xor_b32_e32 v12, 48, v193
	v_xor_b32_e32 v13, 64, v193
	v_xor_b32_e32 v15, 0x50, v193
	v_and_b32_e32 v4, 0x70, v4
	v_lshl_add_u32 v19, v5, 7, s75
	v_or_b32_e32 v206, s3, v5
	v_mov_b32_e32 v5, 0x800
	s_add_i32 s4, s22, 0x7f8
	v_add_u32_e32 v196, 64, v195
	v_add_u32_e32 v198, 64, v197
	v_add_u32_e32 v200, 64, v199
	v_add_u32_e32 v202, 64, v201
	v_lshl_or_b32 v207, v9, 4, v5
	v_writelane_b32 v255, s4, 14
	s_add_i32 s22, s75, 0x2000
	v_add_u32_e32 v210, v194, v6
	v_add_u32_e32 v211, v194, v7
	v_add_u32_e32 v212, v194, v12
	v_add_u32_e32 v213, v194, v13
	v_add_u32_e32 v214, v194, v15
	v_add_u32_e32 v217, v18, v4
	v_add_u32_e32 v218, v20, v4
	v_add_u32_e32 v219, v21, v4
	v_add_u32_e32 v220, v19, v4
	v_mov_b32_e32 v226, 0xff800000
	s_mov_b32 s53, 0
	s_branch .LBB0_431

.LBB0_431:
	s_cmp_lt_i32 s33, 1
	s_cselect_b64 s[78:79], -1, 0
	s_lshl_b32 s37, s88, 6
	ds_read_b128 v[82:85], v221 offset:32768
	ds_read_b128 v[86:89], v222 offset:32768
	ds_read_b128 v[90:93], v223 offset:32768
	ds_read_b128 v[94:97], v224 offset:32768
	ds_read_b128 v[98:101], v221 offset:36864
	ds_read_b128 v[102:105], v222 offset:36864
	ds_read_b128 v[106:109], v223 offset:36864
	ds_read_b128 v[110:113], v224 offset:36864
	s_waitcnt lgkmcnt(7)
	v_mfma_f32_32x32x16_bf16 v[18:33], v[82:85], v[158:161], 0
	s_waitcnt lgkmcnt(6)
	v_mfma_f32_32x32x16_bf16 v[18:33], v[86:89], v[154:157], v[18:33]
	s_waitcnt lgkmcnt(5)
	v_mfma_f32_32x32x16_bf16 v[18:33], v[90:93], v[150:153], v[18:33]
	s_waitcnt lgkmcnt(4)
	v_mfma_f32_32x32x16_bf16 v[18:33], v[94:97], v[146:149], v[18:33]
	ds_read_b128 v[82:85], v221 offset:40960
	ds_read_b128 v[86:89], v222 offset:40960
	ds_read_b128 v[90:93], v223 offset:40960
	ds_read_b128 v[94:97], v224 offset:40960
	s_waitcnt lgkmcnt(7)
	v_mfma_f32_32x32x16_bf16 v[2:17], v[98:101], v[158:161], 0
	s_waitcnt lgkmcnt(6)
	v_mfma_f32_32x32x16_bf16 v[2:17], v[102:105], v[154:157], v[2:17]
	s_waitcnt lgkmcnt(5)
	v_mfma_f32_32x32x16_bf16 v[2:17], v[106:109], v[150:153], v[2:17]
	s_waitcnt lgkmcnt(4)
	v_mfma_f32_32x32x16_bf16 v[2:17], v[110:113], v[146:149], v[2:17]
	ds_read_b128 v[98:101], v221 offset:45056
	ds_read_b128 v[102:105], v222 offset:45056
	ds_read_b128 v[106:109], v223 offset:45056
	ds_read_b128 v[110:113], v224 offset:45056
	s_waitcnt lgkmcnt(7)
	v_mfma_f32_32x32x16_bf16 v[34:49], v[82:85], v[158:161], 0
	s_waitcnt lgkmcnt(6)
	v_mfma_f32_32x32x16_bf16 v[34:49], v[86:89], v[154:157], v[34:49]
	s_waitcnt lgkmcnt(5)
	v_mfma_f32_32x32x16_bf16 v[34:49], v[90:93], v[150:153], v[34:49]
	s_waitcnt lgkmcnt(4)
	v_mfma_f32_32x32x16_bf16 v[34:49], v[94:97], v[146:149], v[34:49]
	ds_read_b128 v[82:85], v221 offset:49152
	ds_read_b128 v[86:89], v222 offset:49152
	ds_read_b128 v[90:93], v223 offset:49152
	ds_read_b128 v[94:97], v224 offset:49152
	s_waitcnt lgkmcnt(7)
	v_mfma_f32_32x32x16_bf16 v[50:65], v[98:101], v[158:161], 0
	s_waitcnt lgkmcnt(6)
	v_mfma_f32_32x32x16_bf16 v[50:65], v[102:105], v[154:157], v[50:65]
	s_waitcnt lgkmcnt(5)
	v_mfma_f32_32x32x16_bf16 v[50:65], v[106:109], v[150:153], v[50:65]
	s_waitcnt lgkmcnt(4)
	v_mfma_f32_32x32x16_bf16 v[50:65], v[110:113], v[146:149], v[50:65]
	s_waitcnt lgkmcnt(3)
	v_mfma_f32_32x32x16_bf16 v[66:81], v[82:85], v[158:161], 0
	s_waitcnt lgkmcnt(2)
	v_mfma_f32_32x32x16_bf16 v[66:81], v[86:89], v[154:157], v[66:81]
	s_waitcnt lgkmcnt(1)
	v_mfma_f32_32x32x16_bf16 v[66:81], v[90:93], v[150:153], v[66:81]
	s_waitcnt lgkmcnt(0)
	v_mfma_f32_32x32x16_bf16 v[66:81], v[94:97], v[146:149], v[66:81]
	s_barrier
	s_add_i32 s38, s53, 1
	s_cmp_lt_i32 s38, s0
	s_cselect_b64 s[96:97], -1, 0
	s_cmp_ge_i32 s38, s0
	s_mov_b32 s39, s86
	s_mov_b32 s40, s88
	s_mov_b32 s47, s81
	s_mov_b32 s41, s33
	s_mov_b32 s80, s42
	s_mov_b32 s48, s82
	v_mov_b32_e32 v183, v180
	v_mov_b32_e32 v190, v178
	v_mov_b32_e32 v187, v182
	s_cbranch_scc1 .LBB0_466
	v_readlane_b32 s40, v254, 8
	v_readlane_b32 s41, v254, 9
	s_mov_b64 s[4:5], -1
	s_and_b64 vcc, exec, s[40:41]
	s_cbranch_vccz .LBB0_454
	s_mul_i32 s4, s38, s74
	v_readlane_b32 s40, v254, 19
	s_add_i32 s39, s4, s40
	s_mov_b64 s[4:5], 0

.LBB0_459:
	s_lshl_b32 s4, s39, 1
	v_readlane_b32 s5, v254, 14
	s_add_i32 s4, s4, s5
	s_ashr_i32 s39, s4, 11
	s_bfe_u32 s5, s4, 0x70004
	s_lshl_b32 s48, s39, 1
	s_and_b32 s40, s4, 15
	s_lshr_b32 s41, s5, s48
	s_bfm_b32 s4, s48, 0
	s_and_b32 s4, s4, s5
	s_lshl_b32 s5, s41, 7
	s_lshl_b32 s5, s5, s48
	s_or_b32 s80, s5, s4
	v_lshlrev_b32_e32 v82, s48, v192
	v_add_u32_e32 v82, s80, v82
	s_movk_i32 s4, 0xc40
	v_mul_lo_u32 v82, v82, s4
	s_lshl_b32 s47, s40, 6
	v_add_lshl_u32 v84, v82, s47, 1
	v_add_u32_e32 v190, v207, v84
.LBB0_461:
.LBB0_462:
.LBB0_464:
.LBB0_465:
	v_lshlrev_b32_e32 v82, s48, v1
	v_add_u32_e32 v183, s80, v82
	v_mov_b64_e32 v[82:83], s[84:85]
	v_mad_i64_i32 v[82:83], s[4:5], v183, s21, v[82:83]
	s_lshl_b32 s90, s47, 1
	v_lshl_add_u64 v[82:83], v[82:83], 0, s[90:91]
	v_mov_b32_e32 v187, v179
	v_lshl_add_u64 v[82:83], v[82:83], 0, v[186:187]
	global_load_dwordx4 v[162:165], v[82:83], off
	global_load_dwordx4 v[166:169], v[82:83], off offset:32
	global_load_dwordx4 v[170:173], v[82:83], off offset:64
	global_load_dwordx4 v[174:177], v[82:83], off offset:96
	s_lshl_b32 s4, 0xffffff80, s48
	s_lshl_b32 s47, 1, s48
	s_add_i32 s48, s80, s4
	v_add_u32_e32 v187, v208, v84
	v_and_b32_e32 v82, 63, v0
	v_lshrrev_b32_e32 v83, 3, v82
	v_and_b32_e32 v86, 7, v82
	v_xor_b32_e32 v86, v86, v83
	v_lshlrev_b32_e32 v86, 4, v86
	s_lshl_b32 s4, s40, 7
	s_add_u32 s4, s4, 0x800
	v_add_u32_e32 v86, s4, v86
	s_bfe_u32 s5, s75, 0x2000c
	s_and_b32 s53, s75, 0xffff0000
	s_add_u32 s53, s53, 0x8000
	s_add_u32 s90, s5, 1
	s_lshl_b32 s4, s90, 5
	v_add_u32_e32 v85, s4, v83
	v_mul_u32_u24_e32 v92, s47, v85
	v_add_u32_e32 v92, s48, v92
	s_lshl_b32 s4, s90, 12
	s_add_u32 s4, s4, s53
	s_lshl_b32 s90, s47, 3
	v_max_i32_e32 v88, 0, v92
	s_mov_b32 m0, s4
	v_mad_u32_u24 v90, v88, s21, v86
	global_load_lds_dwordx4 v90, s[84:85]
	v_add_u32_e32 v92, s90, v92
	v_max_i32_e32 v88, 0, v92
	s_add_u32 m0, s4, 0x400
	v_mad_u32_u24 v90, v88, s21, v86
	global_load_lds_dwordx4 v90, s[84:85]
	v_add_u32_e32 v92, s90, v92
	v_max_i32_e32 v88, 0, v92
	s_add_u32 m0, s4, 0x800
	v_mad_u32_u24 v90, v88, s21, v86
	global_load_lds_dwordx4 v90, s[84:85]
	v_add_u32_e32 v92, s90, v92
	v_max_i32_e32 v88, 0, v92
	s_add_u32 m0, s4, 0xc00
	v_mad_u32_u24 v90, v88, s21, v86
	global_load_lds_dwordx4 v90, s[84:85]
	s_add_u32 s90, s5, 4
	s_cmp_eq_u32 s5, 0
	s_cselect_b32 s90, 0, s90
	s_lshl_b32 s4, s90, 5
	v_add_u32_e32 v85, s4, v83
	v_mul_u32_u24_e32 v92, s47, v85
	v_add_u32_e32 v92, s48, v92
	s_lshl_b32 s4, s90, 12
	s_add_u32 s4, s4, s53
	s_lshl_b32 s90, s47, 3
	v_max_i32_e32 v88, 0, v92
	s_mov_b32 m0, s4
	v_mad_u32_u24 v90, v88, s21, v86
	global_load_lds_dwordx4 v90, s[84:85]
	v_add_u32_e32 v92, s90, v92
	v_max_i32_e32 v88, 0, v92
	s_add_u32 m0, s4, 0x400
	v_mad_u32_u24 v90, v88, s21, v86
	global_load_lds_dwordx4 v90, s[84:85]
	v_add_u32_e32 v92, s90, v92
	v_max_i32_e32 v88, 0, v92
	s_add_u32 m0, s4, 0x800
	v_mad_u32_u24 v90, v88, s21, v86
	global_load_lds_dwordx4 v90, s[84:85]
	v_add_u32_e32 v92, s90, v92
	v_max_i32_e32 v88, 0, v92
	s_add_u32 m0, s4, 0xc00
	v_mad_u32_u24 v90, v88, s21, v86
	global_load_lds_dwordx4 v90, s[84:85]

.LBB0_471:
	v_cndmask_b32_e64 v70, v81, v226, s[78:79]
	v_max3_f32 v33, v18, v97, v20
	v_max3_f32 v33, v33, v19, v22
	v_max3_f32 v33, v33, v21, v24
	v_max3_f32 v33, v33, v23, v26
	v_max3_f32 v33, v33, v25, v28
	v_max3_f32 v33, v33, v27, v31
	v_max3_f32 v33, v33, v29, v30
	v_max3_f32 v33, v33, v32, v3
	v_max3_f32 v33, v33, v2, v5
	v_max3_f32 v33, v33, v4, v7
	v_max3_f32 v33, v33, v6, v9
	v_max3_f32 v33, v33, v8, v11
	v_max3_f32 v33, v33, v10, v13
	v_max3_f32 v33, v33, v12, v15
	v_max3_f32 v33, v33, v14, v17
	v_max3_f32 v33, v33, v16, v35
	v_max3_f32 v33, v33, v34, v37
	v_max3_f32 v33, v33, v36, v39
	v_max3_f32 v33, v33, v38, v41
	v_max3_f32 v33, v33, v40, v43
	v_max3_f32 v33, v33, v42, v45
	v_max3_f32 v33, v33, v44, v47
	v_max3_f32 v33, v33, v46, v49
	v_max3_f32 v33, v33, v48, v51
	v_max3_f32 v33, v33, v50, v53
	v_max3_f32 v33, v33, v52, v55
	v_max3_f32 v33, v33, v54, v57
	v_max3_f32 v33, v33, v56, v59
	v_max3_f32 v33, v33, v58, v61
	v_max3_f32 v33, v33, v60, v63
	v_max3_f32 v33, v33, v62, v65
	v_max3_f32 v33, v33, v64, v83
	v_max3_f32 v33, v33, v82, v85
	v_max3_f32 v33, v33, v84, v87
	v_max3_f32 v33, v33, v86, v89
	v_max3_f32 v33, v33, v88, v91
	v_max3_f32 v33, v33, v90, v93
	v_max3_f32 v33, v33, v92, v95
	v_max3_f32 v33, v33, v94, v70
	v_max_f32_e32 v33, v33, v96
	v_and_b32_e32 v67, 64, v209
	v_xor_b32_e32 v66, 32, v209
	v_add_u32_e32 v67, 64, v67
	v_cmp_lt_i32_e32 vcc, v66, v67
	s_nop 1
	v_cndmask_b32_e32 v66, v209, v66, vcc
	v_lshlrev_b32_e32 v118, 2, v66
	ds_bpermute_b32 v66, v118, v33
	s_waitcnt lgkmcnt(0)
	v_max_f32_e32 v66, v33, v66
	v_pk_add_f32 v[2:3], v[2:3], v[66:67] op_sel_hi:[1,0] neg_lo:[0,1] neg_hi:[0,1]
	v_pk_add_f32 v[4:5], v[4:5], v[66:67] op_sel_hi:[1,0] neg_lo:[0,1] neg_hi:[0,1]
	v_pk_add_f32 v[6:7], v[6:7], v[66:67] op_sel_hi:[1,0] neg_lo:[0,1] neg_hi:[0,1]
	v_pk_add_f32 v[8:9], v[8:9], v[66:67] op_sel_hi:[1,0] neg_lo:[0,1] neg_hi:[0,1]
	v_pk_add_f32 v[10:11], v[10:11], v[66:67] op_sel_hi:[1,0] neg_lo:[0,1] neg_hi:[0,1]
	v_pk_add_f32 v[12:13], v[12:13], v[66:67] op_sel_hi:[1,0] neg_lo:[0,1] neg_hi:[0,1]
	v_pk_add_f32 v[14:15], v[14:15], v[66:67] op_sel_hi:[1,0] neg_lo:[0,1] neg_hi:[0,1]
	v_pk_add_f32 v[16:17], v[16:17], v[66:67] op_sel_hi:[1,0] neg_lo:[0,1] neg_hi:[0,1]
	v_pk_add_f32 v[18:19], v[18:19], v[66:67] op_sel_hi:[1,0] neg_lo:[0,1] neg_hi:[0,1]
	v_pk_add_f32 v[20:21], v[20:21], v[66:67] op_sel_hi:[1,0] neg_lo:[0,1] neg_hi:[0,1]
	v_pk_add_f32 v[22:23], v[22:23], v[66:67] op_sel_hi:[1,0] neg_lo:[0,1] neg_hi:[0,1]
	v_pk_add_f32 v[24:25], v[24:25], v[66:67] op_sel_hi:[1,0] neg_lo:[0,1] neg_hi:[0,1]
	v_pk_add_f32 v[26:27], v[26:27], v[66:67] op_sel_hi:[1,0] neg_lo:[0,1] neg_hi:[0,1]
	v_pk_add_f32 v[28:29], v[28:29], v[66:67] op_sel_hi:[1,0] neg_lo:[0,1] neg_hi:[0,1]
	v_pk_add_f32 v[30:31], v[30:31], v[66:67] op_sel_hi:[1,0] neg_lo:[0,1] neg_hi:[0,1]
	v_pk_add_f32 v[34:35], v[34:35], v[66:67] op_sel_hi:[1,0] neg_lo:[0,1] neg_hi:[0,1]
	v_pk_add_f32 v[36:37], v[36:37], v[66:67] op_sel_hi:[1,0] neg_lo:[0,1] neg_hi:[0,1]
	v_pk_add_f32 v[38:39], v[38:39], v[66:67] op_sel_hi:[1,0] neg_lo:[0,1] neg_hi:[0,1]
	v_pk_add_f32 v[40:41], v[40:41], v[66:67] op_sel_hi:[1,0] neg_lo:[0,1] neg_hi:[0,1]
	v_pk_add_f32 v[42:43], v[42:43], v[66:67] op_sel_hi:[1,0] neg_lo:[0,1] neg_hi:[0,1]
	v_pk_add_f32 v[44:45], v[44:45], v[66:67] op_sel_hi:[1,0] neg_lo:[0,1] neg_hi:[0,1]
	v_pk_add_f32 v[46:47], v[46:47], v[66:67] op_sel_hi:[1,0] neg_lo:[0,1] neg_hi:[0,1]
	v_pk_add_f32 v[48:49], v[48:49], v[66:67] op_sel_hi:[1,0] neg_lo:[0,1] neg_hi:[0,1]
	v_pk_add_f32 v[50:51], v[50:51], v[66:67] op_sel_hi:[1,0] neg_lo:[0,1] neg_hi:[0,1]
	v_pk_add_f32 v[52:53], v[52:53], v[66:67] op_sel_hi:[1,0] neg_lo:[0,1] neg_hi:[0,1]
	v_pk_add_f32 v[54:55], v[54:55], v[66:67] op_sel_hi:[1,0] neg_lo:[0,1] neg_hi:[0,1]
	v_pk_add_f32 v[56:57], v[56:57], v[66:67] op_sel_hi:[1,0] neg_lo:[0,1] neg_hi:[0,1]
	v_pk_add_f32 v[58:59], v[58:59], v[66:67] op_sel_hi:[1,0] neg_lo:[0,1] neg_hi:[0,1]
	v_pk_add_f32 v[60:61], v[60:61], v[66:67] op_sel_hi:[1,0] neg_lo:[0,1] neg_hi:[0,1]
	v_pk_add_f32 v[62:63], v[62:63], v[66:67] op_sel_hi:[1,0] neg_lo:[0,1] neg_hi:[0,1]
	v_pk_add_f32 v[64:65], v[64:65], v[66:67] op_sel_hi:[1,0] neg_lo:[0,1] neg_hi:[0,1]
	v_pk_add_f32 v[82:83], v[82:83], v[66:67] op_sel_hi:[1,0] neg_lo:[0,1] neg_hi:[0,1]
	v_pk_add_f32 v[84:85], v[84:85], v[66:67] op_sel_hi:[1,0] neg_lo:[0,1] neg_hi:[0,1]
	v_pk_add_f32 v[86:87], v[86:87], v[66:67] op_sel_hi:[1,0] neg_lo:[0,1] neg_hi:[0,1]
	v_pk_add_f32 v[88:89], v[88:89], v[66:67] op_sel_hi:[1,0] neg_lo:[0,1] neg_hi:[0,1]
	v_pk_add_f32 v[90:91], v[90:91], v[66:67] op_sel_hi:[1,0] neg_lo:[0,1] neg_hi:[0,1]
	v_pk_add_f32 v[92:93], v[92:93], v[66:67] op_sel_hi:[1,0] neg_lo:[0,1] neg_hi:[0,1]
	v_pk_add_f32 v[94:95], v[94:95], v[66:67] op_sel_hi:[1,0] neg_lo:[0,1] neg_hi:[0,1]
	v_pk_add_f32 v[96:97], v[96:97], v[66:67] op_sel_hi:[1,0] neg_lo:[0,1] neg_hi:[0,1]
	v_sub_f32_e32 v32, v32, v66
	v_sub_f32_e32 v70, v70, v66
	v_exp_f32_e32 v33, v97
	v_exp_f32_e32 v18, v18
	v_exp_f32_e32 v19, v19
	v_exp_f32_e32 v20, v20
	v_add_f32_e32 v67, 0, v33
	v_exp_f32_e32 v21, v21
	v_add_f32_e32 v67, v18, v67
	v_exp_f32_e32 v22, v22
	v_add_f32_e32 v67, v19, v67
	v_exp_f32_e32 v23, v23
	v_add_f32_e32 v67, v20, v67
	v_exp_f32_e32 v24, v24
	v_add_f32_e32 v67, v21, v67
	v_exp_f32_e32 v119, v25
	v_add_f32_e32 v67, v22, v67
	v_exp_f32_e32 v120, v26
	v_add_f32_e32 v67, v23, v67
	v_exp_f32_e32 v121, v27
	v_add_f32_e32 v25, v24, v67
	v_exp_f32_e32 v122, v28
	v_add_f32_e32 v25, v119, v25
	v_exp_f32_e32 v123, v29
	v_add_f32_e32 v25, v120, v25
	v_exp_f32_e32 v124, v31
	v_add_f32_e32 v25, v121, v25
	v_exp_f32_e32 v125, v32
	v_add_f32_e32 v25, v122, v25
	v_exp_f32_e32 v126, v30
	v_add_f32_e32 v25, v123, v25
	v_exp_f32_e32 v103, v2
	v_add_f32_e32 v25, v124, v25
	v_exp_f32_e32 v106, v3
	v_add_f32_e32 v25, v125, v25
	v_exp_f32_e32 v107, v4
	v_add_f32_e32 v2, v126, v25
	v_exp_f32_e32 v110, v5
	v_add_f32_e32 v2, v103, v2
	v_exp_f32_e32 v111, v6
	v_add_f32_e32 v2, v106, v2
	v_exp_f32_e32 v114, v7
	v_add_f32_e32 v2, v107, v2
	v_exp_f32_e32 v115, v8
	v_add_f32_e32 v2, v110, v2
	v_exp_f32_e32 v117, v9
	v_add_f32_e32 v2, v111, v2
	v_exp_f32_e32 v102, v10
	v_add_f32_e32 v2, v114, v2
	v_exp_f32_e32 v104, v11
	v_add_f32_e32 v2, v115, v2
	v_exp_f32_e32 v105, v12
	v_add_f32_e32 v2, v117, v2
	v_exp_f32_e32 v108, v13
	v_add_f32_e32 v2, v102, v2
	v_exp_f32_e32 v109, v14
	v_add_f32_e32 v2, v104, v2
	v_exp_f32_e32 v112, v15
	v_add_f32_e32 v2, v105, v2
	v_exp_f32_e32 v113, v16
	v_add_f32_e32 v2, v108, v2
	v_exp_f32_e32 v116, v17
	v_add_f32_e32 v2, v109, v2
	v_exp_f32_e32 v72, v34
	v_add_f32_e32 v2, v112, v2
	v_exp_f32_e32 v75, v35
	v_add_f32_e32 v2, v113, v2
	v_exp_f32_e32 v76, v36
	v_add_f32_e32 v2, v116, v2
	v_exp_f32_e32 v79, v37
	v_add_f32_e32 v2, v72, v2
	v_exp_f32_e32 v80, v38
	v_add_f32_e32 v2, v75, v2
	v_exp_f32_e32 v98, v39
	v_add_f32_e32 v2, v76, v2
	v_exp_f32_e32 v99, v40
	v_add_f32_e32 v2, v79, v2
	v_exp_f32_e32 v101, v41
	v_add_f32_e32 v2, v80, v2
	v_exp_f32_e32 v71, v42
	v_add_f32_e32 v2, v98, v2
	v_exp_f32_e32 v73, v43
	v_add_f32_e32 v2, v99, v2
	v_exp_f32_e32 v74, v44
	v_add_f32_e32 v2, v101, v2
	v_exp_f32_e32 v77, v45
	v_add_f32_e32 v2, v71, v2
	v_exp_f32_e32 v78, v46
	v_add_f32_e32 v2, v73, v2
	v_exp_f32_e32 v81, v47
	v_add_f32_e32 v2, v74, v2
	v_exp_f32_e32 v97, v48
	v_add_f32_e32 v2, v77, v2
	v_exp_f32_e32 v100, v49
	v_add_f32_e32 v2, v78, v2
	v_exp_f32_e32 v41, v50
	v_add_f32_e32 v2, v81, v2
	v_exp_f32_e32 v46, v51
	v_add_f32_e32 v2, v97, v2
	v_exp_f32_e32 v47, v52
	v_add_f32_e32 v2, v100, v2
	v_exp_f32_e32 v53, v53
	v_add_f32_e32 v2, v41, v2
	v_exp_f32_e32 v54, v54
	v_add_f32_e32 v2, v46, v2
	v_exp_f32_e32 v67, v55
	v_add_f32_e32 v2, v47, v2
	v_exp_f32_e32 v68, v56
	v_add_f32_e32 v2, v53, v2
	v_exp_f32_e32 v69, v57
	v_add_f32_e32 v2, v54, v2
	v_exp_f32_e32 v38, v58
	v_add_f32_e32 v2, v67, v2
	v_exp_f32_e32 v44, v59
	v_add_f32_e32 v2, v68, v2
	v_exp_f32_e32 v45, v60
	v_add_f32_e32 v2, v69, v2
	v_exp_f32_e32 v51, v61
	v_add_f32_e32 v2, v38, v2
	v_exp_f32_e32 v52, v62
	v_add_f32_e32 v2, v44, v2
	v_exp_f32_e32 v57, v63
	v_add_f32_e32 v2, v45, v2
	v_exp_f32_e32 v58, v64
	v_add_f32_e32 v2, v51, v2
	v_exp_f32_e32 v62, v65
	v_add_f32_e32 v2, v52, v2
	v_exp_f32_e32 v37, v82
	v_add_f32_e32 v2, v57, v2
	v_exp_f32_e32 v42, v83
	v_add_f32_e32 v2, v58, v2
	v_exp_f32_e32 v43, v84
	v_add_f32_e32 v2, v62, v2
	v_exp_f32_e32 v49, v85
	v_add_f32_e32 v2, v37, v2
	v_exp_f32_e32 v50, v86
	v_add_f32_e32 v2, v42, v2
	v_exp_f32_e32 v55, v87
	v_add_f32_e32 v2, v43, v2
	v_exp_f32_e32 v56, v88
	v_add_f32_e32 v2, v49, v2
	v_exp_f32_e32 v61, v89
	v_add_f32_e32 v2, v50, v2
	v_exp_f32_e32 v36, v90
	v_add_f32_e32 v2, v55, v2
	v_exp_f32_e32 v39, v91
	v_add_f32_e32 v2, v56, v2
	v_exp_f32_e32 v40, v92
	v_add_f32_e32 v2, v61, v2
	v_add_f32_e32 v2, v36, v2
	v_add_f32_e32 v2, v39, v2
	v_add_f32_e32 v14, v40, v2
	v_exp_f32_e32 v48, v93
	v_cvt_pk_bf16_f32 v2, v33, v18
	v_cvt_pk_bf16_f32 v3, v19, v20
	v_cvt_pk_bf16_f32 v4, v21, v22
	v_cvt_pk_bf16_f32 v5, v23, v24
	s_bitcmp1_b32 s96, 0
	s_cbranch_scc1 .Latt_b3m
	s_waitcnt vmcnt(0)

.LBB0_473:
.LBB0_475:
	s_nop 0
	v_cvt_pk_bf16_f32 v82, v103, v106
	v_cvt_pk_bf16_f32 v83, v107, v110
	v_cvt_pk_bf16_f32 v84, v111, v114
	v_cvt_pk_bf16_f32 v85, v115, v117
	s_waitcnt lgkmcnt(0)
	ds_read_b64_tr_b16 v[236:237], v201
	ds_read_b64_tr_b16 v[238:239], v201 offset:1024
	ds_read_b64_tr_b16 v[240:241], v202
	ds_read_b64_tr_b16 v[242:243], v202 offset:1024
	s_nop 0
	v_mfma_f32_32x32x16_bf16 v[18:33], v[228:231], v[82:85], v[18:33]
	v_mfma_f32_32x32x16_bf16 v[2:17], v[232:235], v[82:85], v[2:17]
	v_cvt_pk_bf16_f32 v82, v102, v104
	v_cvt_pk_bf16_f32 v83, v105, v108
	v_cvt_pk_bf16_f32 v84, v109, v112
	v_cvt_pk_bf16_f32 v85, v113, v116
	s_waitcnt lgkmcnt(0)
	ds_read_b64_tr_b16 v[228:229], v195 offset:8192
	ds_read_b64_tr_b16 v[230:231], v195 offset:9216
	ds_read_b64_tr_b16 v[232:233], v196 offset:8192
	ds_read_b64_tr_b16 v[234:235], v196 offset:9216
	s_nop 0
	v_mfma_f32_32x32x16_bf16 v[18:33], v[236:239], v[82:85], v[18:33]
	v_mfma_f32_32x32x16_bf16 v[2:17], v[240:243], v[82:85], v[2:17]
.LBB0_477:
.LBB0_479:
	s_nop 0
	v_cvt_pk_bf16_f32 v82, v72, v75
	v_cvt_pk_bf16_f32 v83, v76, v79
	v_cvt_pk_bf16_f32 v84, v80, v98
	v_cvt_pk_bf16_f32 v85, v99, v101
	s_waitcnt lgkmcnt(0)
	ds_read_b64_tr_b16 v[236:237], v197 offset:8192
	ds_read_b64_tr_b16 v[238:239], v197 offset:9216
	ds_read_b64_tr_b16 v[240:241], v198 offset:8192
	ds_read_b64_tr_b16 v[242:243], v198 offset:9216
	v_cvt_pk_bf16_f32 v72, v71, v73
	v_cvt_pk_bf16_f32 v73, v74, v77
	v_cvt_pk_bf16_f32 v74, v78, v81
	v_cvt_pk_bf16_f32 v75, v97, v100
	s_nop 0
	v_mfma_f32_32x32x16_bf16 v[18:33], v[228:231], v[82:85], v[18:33]
	v_mfma_f32_32x32x16_bf16 v[2:17], v[232:235], v[82:85], v[2:17]
	s_waitcnt lgkmcnt(0)
	ds_read_b64_tr_b16 v[228:229], v199 offset:8192
	ds_read_b64_tr_b16 v[230:231], v199 offset:9216
	ds_read_b64_tr_b16 v[232:233], v200 offset:8192
	ds_read_b64_tr_b16 v[234:235], v200 offset:9216
	s_nop 0
	v_mfma_f32_32x32x16_bf16 v[18:33], v[236:239], v[72:75], v[18:33]
	v_mfma_f32_32x32x16_bf16 v[2:17], v[240:243], v[72:75], v[2:17]
.LBB0_481:
.LBB0_483:
	s_andn2_b64 vcc, exec, s[96:97]
	v_cvt_pk_bf16_f32 v72, v41, v46
	v_cvt_pk_bf16_f32 v73, v47, v53
	v_cvt_pk_bf16_f32 v74, v54, v67
	v_cvt_pk_bf16_f32 v75, v68, v69
	s_waitcnt lgkmcnt(0)
	ds_read_b64_tr_b16 v[236:237], v201 offset:8192
	ds_read_b64_tr_b16 v[238:239], v201 offset:9216
	ds_read_b64_tr_b16 v[240:241], v202 offset:8192
	ds_read_b64_tr_b16 v[242:243], v202 offset:9216
	v_cvt_pk_bf16_f32 v44, v38, v44
	v_cvt_pk_bf16_f32 v45, v45, v51
	v_cvt_pk_bf16_f32 v46, v52, v57
	v_cvt_pk_bf16_f32 v47, v58, v62
	s_nop 0
	v_mfma_f32_32x32x16_bf16 v[18:33], v[228:231], v[72:75], v[18:33]
	v_mfma_f32_32x32x16_bf16 v[2:17], v[232:235], v[72:75], v[2:17]
	s_waitcnt lgkmcnt(0)
	ds_read_b64_tr_b16 v[228:229], v195 offset:16384
	ds_read_b64_tr_b16 v[230:231], v195 offset:17408
	ds_read_b64_tr_b16 v[232:233], v196 offset:16384
	ds_read_b64_tr_b16 v[234:235], v196 offset:17408
	v_cvt_pk_bf16_f32 v42, v37, v42
	v_cvt_pk_bf16_f32 v43, v43, v49
	s_nop 0
	v_mfma_f32_32x32x16_bf16 v[18:33], v[236:239], v[44:47], v[18:33]
	v_mfma_f32_32x32x16_bf16 v[2:17], v[240:243], v[44:47], v[2:17]
	v_cvt_pk_bf16_f32 v44, v50, v55
	v_cvt_pk_bf16_f32 v45, v56, v61
	s_waitcnt lgkmcnt(0)
	ds_read_b64_tr_b16 v[236:237], v197 offset:16384
	ds_read_b64_tr_b16 v[238:239], v197 offset:17408
	ds_read_b64_tr_b16 v[240:241], v198 offset:16384
	ds_read_b64_tr_b16 v[242:243], v198 offset:17408
	v_cvt_pk_bf16_f32 v34, v36, v39
	v_cvt_pk_bf16_f32 v35, v40, v48
	v_cvt_pk_bf16_f32 v36, v63, v65
	v_cvt_pk_bf16_f32 v37, v64, v70
	s_nop 0
	v_mfma_f32_32x32x16_bf16 v[18:33], v[228:231], v[42:45], v[18:33]
	v_mfma_f32_32x32x16_bf16 v[2:17], v[232:235], v[42:45], v[2:17]
	s_waitcnt lgkmcnt(0)
	s_nop 0
	v_mfma_f32_32x32x16_bf16 v[18:33], v[236:239], v[34:37], v[18:33]
	v_cndmask_b32_e64 v42, 0, 1, s[96:97]
	v_cmp_ne_u32_e64 s[72:73], 1, v42
	v_mfma_f32_32x32x16_bf16 v[2:17], v[240:243], v[34:37], v[2:17]
	s_cbranch_vccnz .LBB0_485
	s_waitcnt vmcnt(0)
